# speedup vs baseline: 1.0019x; 1.0019x over previous
.LBB0_15:
	s_cmp_gt_u32 s3, 3
	s_cselect_b64 vcc, -1, 0
	s_and_b64 s[14:15], vcc, exec
	s_waitcnt vmcnt(8)
	v_cndmask_b32_e32 v176, v236, v1, vcc
	s_cselect_b32 s55, 0x20000, 0x20000
	s_cselect_b32 s54, s16, 0x8000000
	s_cselect_b32 s53, s41, s37
	s_cselect_b32 s52, s22, s36
	buffer_load_dwordx4 v[148:151], v176, s[52:55], 0 offen nt
	buffer_load_dwordx4 v[152:155], v176, s[52:55], 0 offen offset:512 nt
	buffer_load_dwordx4 v[164:167], v176, s[52:55], 0 offen offset:1024 nt
	buffer_load_dwordx4 v[156:159], v176, s[52:55], 0 offen offset:1536 nt
	buffer_load_dwordx4 v[160:163], v176, s[52:55], 0 offen offset:2048 nt
	buffer_load_dwordx4 v[168:171], v176, s[52:55], 0 offen offset:2560 nt
	buffer_load_dwordx4 v[172:175], v176, s[52:55], 0 offen offset:3072 nt
	s_nop 0
	buffer_load_dwordx4 v[176:179], v176, s[52:55], 0 offen offset:3584 nt
	s_add_i32 s3, s3, 2
	ds_read_b128 v[180:183], v235 offset:32768
	ds_read_b128 v[184:187], v233 offset:32768
	ds_read_b128 v[188:191], v233 offset:33792
	ds_read_b128 v[192:195], v235 offset:36864
	v_add_u32_e32 v236, 0x20000, v236
	s_waitcnt lgkmcnt(3)
	v_dot2c_f32_f16_e32 v217, 0x3c003c00, v180
	s_waitcnt lgkmcnt(2)
	v_mfma_f32_32x32x16_f16 v[18:33], v[180:183], v[184:187], v[18:33]
	v_dot2c_f32_f16_e32 v217, 0x3c003c00, v181
	v_dot2c_f32_f16_e32 v217, 0x3c003c00, v182
	v_dot2c_f32_f16_e32 v217, 0x3c003c00, v183
	s_waitcnt lgkmcnt(0)
	v_dot2c_f32_f16_e32 v217, 0x3c003c00, v192
	v_dot2c_f32_f16_e32 v217, 0x3c003c00, v193
	v_dot2c_f32_f16_e32 v217, 0x3c003c00, v194
	v_dot2c_f32_f16_e32 v217, 0x3c003c00, v195
	v_mfma_f32_32x32x16_f16 v[2:17], v[180:183], v[188:191], v[2:17]
	ds_read_b128 v[184:187], v233 offset:36864
	ds_read_b128 v[188:191], v233 offset:37888
	s_and_b64 vcc, exec, s[12:13]
	s_waitcnt lgkmcnt(1)
	v_mfma_f32_32x32x16_f16 v[18:33], v[192:195], v[184:187], v[18:33]
	s_waitcnt lgkmcnt(0)
	v_mfma_f32_32x32x16_f16 v[2:17], v[192:195], v[188:191], v[2:17]
	ds_read_b128 v[184:187], v235 offset:40960
	ds_read_b128 v[188:191], v233 offset:40960
	ds_read_b128 v[196:199], v233 offset:41984
	ds_read_b128 v[200:203], v235 offset:45056
	s_waitcnt lgkmcnt(3)
	v_dot2c_f32_f16_e32 v217, 0x3c003c00, v184
	v_dot2c_f32_f16_e32 v217, 0x3c003c00, v185
	v_dot2c_f32_f16_e32 v217, 0x3c003c00, v186
	v_dot2c_f32_f16_e32 v217, 0x3c003c00, v187
	s_waitcnt lgkmcnt(0)
	v_dot2c_f32_f16_e32 v217, 0x3c003c00, v200
	v_mfma_f32_32x32x16_f16 v[18:33], v[184:187], v[188:191], v[18:33]
	v_dot2c_f32_f16_e32 v217, 0x3c003c00, v201
	v_dot2c_f32_f16_e32 v217, 0x3c003c00, v202
	v_dot2c_f32_f16_e32 v217, 0x3c003c00, v203
	v_mfma_f32_32x32x16_f16 v[2:17], v[184:187], v[196:199], v[2:17]
	ds_read_b128 v[188:191], v233 offset:45056
	ds_read_b128 v[196:199], v233 offset:46080
	s_waitcnt lgkmcnt(1)
	v_mfma_f32_32x32x16_f16 v[18:33], v[200:203], v[188:191], v[18:33]
	s_waitcnt lgkmcnt(0)
	v_mfma_f32_32x32x16_f16 v[2:17], v[200:203], v[196:199], v[2:17]
	ds_read_b128 v[188:191], v235 offset:49152
	ds_read_b128 v[196:199], v233 offset:49152
	ds_read_b128 v[204:207], v233 offset:50176
	ds_read_b128 v[208:211], v235 offset:53248
	ds_read_b128 v[180:183], v233 offset:54272
	ds_read_b128 v[192:195], v235 offset:57344
	s_waitcnt lgkmcnt(5)
	v_dot2c_f32_f16_e32 v217, 0x3c003c00, v188
	v_dot2c_f32_f16_e32 v217, 0x3c003c00, v189
	v_dot2c_f32_f16_e32 v217, 0x3c003c00, v190
	v_dot2c_f32_f16_e32 v217, 0x3c003c00, v191
	s_waitcnt lgkmcnt(4)
	v_mfma_f32_32x32x16_f16 v[18:33], v[188:191], v[196:199], v[18:33]
	ds_read_b128 v[196:199], v233 offset:53248
	s_waitcnt lgkmcnt(3)
	v_dot2c_f32_f16_e32 v217, 0x3c003c00, v208
	v_dot2c_f32_f16_e32 v217, 0x3c003c00, v209
	v_dot2c_f32_f16_e32 v217, 0x3c003c00, v210
	v_dot2c_f32_f16_e32 v217, 0x3c003c00, v211
	v_mfma_f32_32x32x16_f16 v[2:17], v[188:191], v[204:207], v[2:17]
	s_waitcnt lgkmcnt(0)
	v_mfma_f32_32x32x16_f16 v[18:33], v[208:211], v[196:199], v[18:33]
	v_mfma_f32_32x32x16_f16 v[2:17], v[208:211], v[180:183], v[2:17]
	ds_read_b128 v[180:183], v233 offset:57344
	ds_read_b128 v[184:187], v233 offset:58368
	ds_read_b128 v[196:199], v235 offset:61440
	v_dot2c_f32_f16_e32 v217, 0x3c003c00, v192
	v_dot2c_f32_f16_e32 v217, 0x3c003c00, v193
	v_dot2c_f32_f16_e32 v217, 0x3c003c00, v194
	v_dot2c_f32_f16_e32 v217, 0x3c003c00, v195
	s_waitcnt lgkmcnt(0)
	v_dot2c_f32_f16_e32 v217, 0x3c003c00, v196
	v_mfma_f32_32x32x16_f16 v[18:33], v[192:195], v[180:183], v[18:33]
	ds_read_b128 v[180:183], v233 offset:61440
	v_dot2c_f32_f16_e32 v217, 0x3c003c00, v197
	v_dot2c_f32_f16_e32 v217, 0x3c003c00, v198
	v_dot2c_f32_f16_e32 v217, 0x3c003c00, v199
	v_mfma_f32_32x32x16_f16 v[2:17], v[192:195], v[184:187], v[2:17]
	ds_read_b128 v[184:187], v233 offset:62464
	s_waitcnt lgkmcnt(1)
	v_mfma_f32_32x32x16_f16 v[18:33], v[196:199], v[180:183], v[18:33]
	s_waitcnt lgkmcnt(0)
	v_mfma_f32_32x32x16_f16 v[2:17], v[196:199], v[184:187], v[2:17]
	s_cbranch_vccnz .LBB0_19

.Lw03_wdone:
	v_cvt_pk_f16_f32 v183, v140, v144
	v_cvt_pk_f16_f32 v182, v132, v136
	v_cvt_pk_f16_f32 v181, v124, v128
	v_cvt_pk_f16_f32 v180, v116, v120
	v_cvt_pk_f16_f32 v187, v141, v145
	v_cvt_pk_f16_f32 v186, v133, v137
	v_cvt_pk_f16_f32 v185, v125, v129
	v_cvt_pk_f16_f32 v184, v117, v121
	v_cvt_pk_f16_f32 v191, v142, v146
	v_cvt_pk_f16_f32 v190, v134, v138
	v_cvt_pk_f16_f32 v189, v126, v130
	v_cvt_pk_f16_f32 v188, v118, v122
	v_cvt_pk_f16_f32 v195, v143, v147
	v_cvt_pk_f16_f32 v194, v135, v139
	v_cvt_pk_f16_f32 v193, v127, v131
	v_cvt_pk_f16_f32 v192, v119, v123
	buffer_load_dwordx4 v[116:119], v196, s[12:15], 0 offen nt
	buffer_load_dwordx4 v[120:123], v196, s[12:15], 0 offen offset:512 nt
	buffer_load_dwordx4 v[124:127], v196, s[12:15], 0 offen offset:1024 nt
	buffer_load_dwordx4 v[128:131], v196, s[12:15], 0 offen offset:1536 nt
	buffer_load_dwordx4 v[132:135], v196, s[12:15], 0 offen offset:2048 nt
	buffer_load_dwordx4 v[136:139], v196, s[12:15], 0 offen offset:2560 nt
	buffer_load_dwordx4 v[140:143], v196, s[12:15], 0 offen offset:3072 nt
	buffer_load_dwordx4 v[144:147], v196, s[12:15], 0 offen offset:3584 nt
	ds_write_b128 v234, v[180:183] offset:32768
	ds_write_b128 v234, v[184:187] offset:33792
	ds_write_b128 v234, v[188:191] offset:34816
	ds_write_b128 v234, v[192:195] offset:35840
	ds_read_b128 v[180:183], v235
	ds_read_b128 v[188:191], v233
	ds_read_b128 v[192:195], v233 offset:1024
	ds_read_b128 v[184:187], v235 offset:4096
	s_waitcnt lgkmcnt(2)
	v_mfma_f32_32x32x16_f16 v[18:33], v[180:183], v[188:191], v[18:33]
	s_waitcnt lgkmcnt(1)
	v_mfma_f32_32x32x16_f16 v[2:17], v[180:183], v[192:195], v[2:17]
	ds_read_b128 v[188:191], v233 offset:4096
	ds_read_b128 v[192:195], v233 offset:5120
	s_waitcnt lgkmcnt(1)
	v_mfma_f32_32x32x16_f16 v[18:33], v[184:187], v[188:191], v[18:33]
	s_waitcnt lgkmcnt(0)
	v_mfma_f32_32x32x16_f16 v[2:17], v[184:187], v[192:195], v[2:17]
	ds_read_b128 v[188:191], v235 offset:8192
	ds_read_b128 v[196:199], v233 offset:8192
	ds_read_b128 v[200:203], v233 offset:9216
	ds_read_b128 v[192:195], v235 offset:12288
	s_waitcnt lgkmcnt(2)
	v_mfma_f32_32x32x16_f16 v[18:33], v[188:191], v[196:199], v[18:33]
	s_waitcnt lgkmcnt(1)
	v_mfma_f32_32x32x16_f16 v[2:17], v[188:191], v[200:203], v[2:17]
	ds_read_b128 v[196:199], v233 offset:12288
	ds_read_b128 v[200:203], v233 offset:13312
	s_waitcnt lgkmcnt(1)
	v_mfma_f32_32x32x16_f16 v[18:33], v[192:195], v[196:199], v[18:33]
	s_waitcnt lgkmcnt(0)
	v_mfma_f32_32x32x16_f16 v[2:17], v[192:195], v[200:203], v[2:17]
	ds_read_b128 v[196:199], v235 offset:16384
	ds_read_b128 v[204:207], v233 offset:16384
	ds_read_b128 v[208:211], v233 offset:17408
	ds_read_b128 v[200:203], v235 offset:20480
	s_waitcnt lgkmcnt(2)
	v_mfma_f32_32x32x16_f16 v[18:33], v[196:199], v[204:207], v[18:33]
	s_waitcnt lgkmcnt(1)
	v_mfma_f32_32x32x16_f16 v[2:17], v[196:199], v[208:211], v[2:17]
	ds_read_b128 v[204:207], v233 offset:20480
	ds_read_b128 v[208:211], v233 offset:21504
	s_waitcnt lgkmcnt(1)
	v_mfma_f32_32x32x16_f16 v[18:33], v[200:203], v[204:207], v[18:33]
	s_waitcnt lgkmcnt(0)
	v_mfma_f32_32x32x16_f16 v[2:17], v[200:203], v[208:211], v[2:17]
	ds_read_b128 v[204:207], v235 offset:24576
	ds_read_b128 v[238:241], v233 offset:24576
	ds_read_b128 v[242:245], v233 offset:25600
	ds_read_b128 v[208:211], v235 offset:28672
	s_waitcnt lgkmcnt(2)
	v_mfma_f32_32x32x16_f16 v[18:33], v[204:207], v[238:241], v[18:33]
	s_waitcnt lgkmcnt(1)
	v_mfma_f32_32x32x16_f16 v[2:17], v[204:207], v[242:245], v[2:17]
	ds_read_b128 v[238:241], v233 offset:28672
	ds_read_b128 v[242:245], v233 offset:29696
	s_waitcnt lgkmcnt(1)
	v_mfma_f32_32x32x16_f16 v[18:33], v[208:211], v[238:241], v[18:33]
	s_waitcnt lgkmcnt(0)
	v_mfma_f32_32x32x16_f16 v[2:17], v[208:211], v[242:245], v[2:17]
	v_dot2c_f32_f16_e32 v217, 0x3c003c00, v180
	v_dot2c_f32_f16_e32 v217, 0x3c003c00, v181
	v_dot2c_f32_f16_e32 v217, 0x3c003c00, v182
	v_dot2c_f32_f16_e32 v217, 0x3c003c00, v183
	v_dot2c_f32_f16_e32 v217, 0x3c003c00, v184
	v_dot2c_f32_f16_e32 v217, 0x3c003c00, v185
	v_dot2c_f32_f16_e32 v217, 0x3c003c00, v186
	v_dot2c_f32_f16_e32 v217, 0x3c003c00, v187
	v_dot2c_f32_f16_e32 v217, 0x3c003c00, v188
	v_dot2c_f32_f16_e32 v217, 0x3c003c00, v189
	v_dot2c_f32_f16_e32 v217, 0x3c003c00, v190
	v_dot2c_f32_f16_e32 v217, 0x3c003c00, v191
	v_dot2c_f32_f16_e32 v217, 0x3c003c00, v192
	v_dot2c_f32_f16_e32 v217, 0x3c003c00, v193
	v_dot2c_f32_f16_e32 v217, 0x3c003c00, v194
	v_dot2c_f32_f16_e32 v217, 0x3c003c00, v195
	v_dot2c_f32_f16_e32 v217, 0x3c003c00, v196
	v_dot2c_f32_f16_e32 v217, 0x3c003c00, v197
	v_dot2c_f32_f16_e32 v217, 0x3c003c00, v198
	v_dot2c_f32_f16_e32 v217, 0x3c003c00, v199
	v_dot2c_f32_f16_e32 v217, 0x3c003c00, v200
	v_dot2c_f32_f16_e32 v217, 0x3c003c00, v201
	v_dot2c_f32_f16_e32 v217, 0x3c003c00, v202
	v_dot2c_f32_f16_e32 v217, 0x3c003c00, v203
	v_dot2c_f32_f16_e32 v217, 0x3c003c00, v204
	v_dot2c_f32_f16_e32 v217, 0x3c003c00, v205
	v_dot2c_f32_f16_e32 v217, 0x3c003c00, v206
	v_dot2c_f32_f16_e32 v217, 0x3c003c00, v207
	v_dot2c_f32_f16_e32 v217, 0x3c003c00, v208
	v_dot2c_f32_f16_e32 v217, 0x3c003c00, v209
	v_dot2c_f32_f16_e32 v217, 0x3c003c00, v210
	v_dot2c_f32_f16_e32 v217, 0x3c003c00, v211
	s_cmp_gt_u32 s3, 5
	s_cselect_b64 s[12:13], -1, 0
	s_and_b64 vcc, exec, s[12:13]
	s_barrier
	s_cbranch_vccnz .LBB0_15
	s_waitcnt vmcnt(8)
	v_cvt_pk_f16_f32 v241, v172, v176
	v_cvt_pk_f16_f32 v240, v160, v168
	v_cvt_pk_f16_f32 v239, v164, v156
	v_cvt_pk_f16_f32 v238, v148, v152
	ds_write_b128 v234, v[238:241]
	v_cvt_pk_f16_f32 v241, v173, v177
	v_cvt_pk_f16_f32 v240, v161, v169
	v_cvt_pk_f16_f32 v239, v165, v157
	v_cvt_pk_f16_f32 v238, v149, v153
	ds_write_b128 v234, v[238:241] offset:1024
	v_cvt_pk_f16_f32 v241, v174, v178
	v_cvt_pk_f16_f32 v240, v162, v170
	v_cvt_pk_f16_f32 v239, v166, v158
	v_cvt_pk_f16_f32 v238, v150, v154
	v_cvt_pk_f16_f32 v161, v175, v179
	v_cvt_pk_f16_f32 v160, v163, v171
	v_cvt_pk_f16_f32 v159, v167, v159
	v_cvt_pk_f16_f32 v158, v151, v155
	ds_write_b128 v234, v[238:241] offset:2048
	ds_write_b128 v234, v[158:161] offset:3072
	s_cmp_lg_u32 s3, 0
	s_cbranch_scc1 .LBB0_15
	v_cvt_pk_f16_f32 v48, v48, v49
	v_cvt_pk_f16_f32 v49, v50, v51
	ds_write_b64 v246, v[48:49]
	v_cvt_pk_f16_f32 v80, v80, v81
	v_cvt_pk_f16_f32 v81, v82, v83
	ds_write_b64 v246, v[80:81] offset:34816
	v_cvt_pk_f16_f32 v52, v52, v53
	v_cvt_pk_f16_f32 v53, v54, v55
	ds_write_b64 v246, v[52:53] offset:4352
	v_cvt_pk_f16_f32 v84, v84, v85
	v_cvt_pk_f16_f32 v85, v86, v87
	ds_write_b64 v246, v[84:85] offset:39168
	v_cvt_pk_f16_f32 v56, v56, v57
	v_cvt_pk_f16_f32 v57, v58, v59
	ds_write_b64 v246, v[56:57] offset:8704
	v_cvt_pk_f16_f32 v88, v88, v89
	v_cvt_pk_f16_f32 v89, v90, v91
	ds_write_b64 v246, v[88:89] offset:43520
	v_cvt_pk_f16_f32 v60, v60, v61
	v_cvt_pk_f16_f32 v61, v62, v63
	ds_write_b64 v246, v[60:61] offset:13056
	v_cvt_pk_f16_f32 v92, v92, v93
	v_cvt_pk_f16_f32 v93, v94, v95
	ds_write_b64 v246, v[92:93] offset:47872
	v_cvt_pk_f16_f32 v64, v64, v65
	v_cvt_pk_f16_f32 v65, v66, v67
	ds_write_b64 v246, v[64:65] offset:17408
	v_cvt_pk_f16_f32 v96, v96, v97
	v_cvt_pk_f16_f32 v97, v98, v99
	ds_write_b64 v246, v[96:97] offset:52224
	v_cvt_pk_f16_f32 v68, v68, v69
	v_cvt_pk_f16_f32 v69, v70, v71
	ds_write_b64 v246, v[68:69] offset:21760
	v_cvt_pk_f16_f32 v100, v100, v101
	v_cvt_pk_f16_f32 v101, v102, v103
	ds_write_b64 v246, v[100:101] offset:56576
	v_cvt_pk_f16_f32 v72, v72, v73
	v_cvt_pk_f16_f32 v73, v74, v75
	ds_write_b64 v246, v[72:73] offset:26112
	v_cvt_pk_f16_f32 v104, v104, v105
	v_cvt_pk_f16_f32 v105, v106, v107
	ds_write_b64 v246, v[104:105] offset:60928
	v_cvt_pk_f16_f32 v76, v76, v77
	v_cvt_pk_f16_f32 v77, v78, v79
	ds_write_b64 v246, v[76:77] offset:30464
	v_cvt_pk_f16_f32 v108, v108, v109
	v_cvt_pk_f16_f32 v109, v110, v111
	ds_write_b64 v246, v[108:109] offset:65280
	s_branch .LBB0_15
